# baseline (speedup 1.0000x reference)
_Z9ssim_mainPKfS0_S0_Pf:
	v_readfirstlane_b32 s29, v0
	s_load_dwordx4 s[4:7], s[0:1], 0x0
	s_load_dwordx4 s[8:11], s[0:1], 0x10
	s_mov_b32 s51, 0x44800000
	s_mov_b32 s38, 0
	s_mov_b32 s39, -1
	s_lshr_b32 s12, s29, 6
	s_mov_b32 s13, s2
	s_lshr_b32 s14, s13, 3
	s_and_b32 s15, s13, 7
	s_lshl_b32 s16, s14, 20
	s_lshl_b32 s17, s15, 17
	s_add_u32 s16, s16, s17
	s_lshl_b32 s17, s12, 8
	s_add_u32 s16, s16, s17
	s_lshl_b32 s27, s12, 2
	s_add_u32 s27, s27, 0x10000
	v_and_b32_e32 v8, 63, v0
	v_and_b32_e32 v169, 15, v0
	v_bfe_u32 v164, v0, 4, 2
	v_lshrrev_b32_e32 v167, 2, v169
	v_lshlrev_b32_e32 v167, 5, v167
	v_and_b32_e32 v168, 1, v169
	v_lshl_or_b32 v167, v168, 4, v167
	v_bfe_u32 v168, v169, 1, 1
	v_lshl_or_b32 v167, v168, 7, v167
	v_lshl_or_b32 v9, v164, 14, v167
	v_and_b32_e32 v168, 1, v164
	v_lshl_or_b32 v23, v168, 14, v167
	v_lshrrev_b32_e32 v168, 1, v164
	v_lshl_or_b32 v23, v168, 13, v23
	v_add_u32_e32 v237, 0x1000, v9
	v_add_u32_e32 v238, 0x2000, v9
	v_add_u32_e32 v239, 0x3000, v9
	v_add_u32_e32 v240, 0x10000, v9
	v_add_u32_e32 v241, 0x11000, v9
	v_add_u32_e32 v242, 0x12000, v9
	v_add_u32_e32 v243, 0x13000, v9
	s_waitcnt lgkmcnt(0)
	s_load_dwordx8 s[40:47], s[8:9], 0x0
	s_load_dwordx2 s[48:49], s[8:9], 0x20
	s_load_dword s50, s[8:9], 0x28
	s_add_u32 s18, s4, s16
	s_addc_u32 s19, s5, 0
	s_add_u32 s20, s6, s16
	s_addc_u32 s21, s7, 0
	global_load_dwordx4 v[36:39], v9, s[18:19] offset:0 sc1 nt
	global_load_dwordx4 v[40:43], v9, s[18:19] offset:2048 sc1 nt
	global_load_dwordx4 v[68:71], v9, s[20:21] offset:0 sc1 nt
	global_load_dwordx4 v[72:75], v9, s[20:21] offset:2048 sc1 nt
	global_load_dwordx4 v[44:47], v237, s[18:19] offset:0 sc1 nt
	global_load_dwordx4 v[48:51], v237, s[18:19] offset:2048 sc1 nt
	global_load_dwordx4 v[76:79], v237, s[20:21] offset:0 sc1 nt
	global_load_dwordx4 v[80:83], v237, s[20:21] offset:2048 sc1 nt
	global_load_dwordx4 v[52:55], v238, s[18:19] offset:0 sc1 nt
	global_load_dwordx4 v[56:59], v238, s[18:19] offset:2048 sc1 nt
	global_load_dwordx4 v[84:87], v238, s[20:21] offset:0 sc1 nt
	global_load_dwordx4 v[88:91], v238, s[20:21] offset:2048 sc1 nt
	global_load_dwordx4 v[60:63], v239, s[18:19] offset:0 sc1 nt
	global_load_dwordx4 v[64:67], v239, s[18:19] offset:2048 sc1 nt
	global_load_dwordx4 v[92:95], v239, s[20:21] offset:0 sc1 nt
	global_load_dwordx4 v[96:99], v239, s[20:21] offset:2048 sc1 nt
	v_mov_b32_e32 v6, s27
	v_mov_b32_e32 v168, 0
	ds_write_b32 v6, v168 offset:0
	ds_write_b32 v6, v168 offset:32
	ds_write_b32 v6, v168 offset:64
	ds_write_b32 v6, v168 offset:96
	v_lshlrev_b32_e32 v167, 3, v164
	v_xor_b32_e32 v168, 16, v167
	v_sub_u32_e32 v165, v167, v169
	v_sub_u32_e32 v166, v168, v169
	v_add_u32_e32 v172, 0, v165
	v_min_u32_e32 v172, 11, v172
	v_lshlrev_b32_e32 v172, 2, v172
	v_add_u32_e32 v173, 1, v165
	v_min_u32_e32 v173, 11, v173
	v_lshlrev_b32_e32 v173, 2, v173
	v_add_u32_e32 v174, 2, v165
	v_min_u32_e32 v174, 11, v174
	v_lshlrev_b32_e32 v174, 2, v174
	v_add_u32_e32 v175, 3, v165
	v_min_u32_e32 v175, 11, v175
	v_lshlrev_b32_e32 v175, 2, v175
	v_add_u32_e32 v176, 4, v165
	v_min_u32_e32 v176, 11, v176
	v_lshlrev_b32_e32 v176, 2, v176
	v_add_u32_e32 v177, 5, v165
	v_min_u32_e32 v177, 11, v177
	v_lshlrev_b32_e32 v177, 2, v177
	v_add_u32_e32 v178, 6, v165
	v_min_u32_e32 v178, 11, v178
	v_lshlrev_b32_e32 v178, 2, v178
	v_add_u32_e32 v179, 7, v165
	v_min_u32_e32 v179, 11, v179
	v_lshlrev_b32_e32 v179, 2, v179
	v_add_u32_e32 v180, 0, v166
	v_min_u32_e32 v180, 11, v180
	v_lshlrev_b32_e32 v180, 2, v180
	v_add_u32_e32 v181, 1, v166
	v_min_u32_e32 v181, 11, v181
	v_lshlrev_b32_e32 v181, 2, v181
	v_add_u32_e32 v182, 2, v166
	v_min_u32_e32 v182, 11, v182
	v_lshlrev_b32_e32 v182, 2, v182
	v_add_u32_e32 v183, 3, v166
	v_min_u32_e32 v183, 11, v183
	v_lshlrev_b32_e32 v183, 2, v183
	v_add_u32_e32 v184, 4, v166
	v_min_u32_e32 v184, 11, v184
	v_lshlrev_b32_e32 v184, 2, v184
	v_add_u32_e32 v185, 5, v166
	v_min_u32_e32 v185, 11, v185
	v_lshlrev_b32_e32 v185, 2, v185
	v_add_u32_e32 v186, 6, v166
	v_min_u32_e32 v186, 11, v186
	v_lshlrev_b32_e32 v186, 2, v186
	v_add_u32_e32 v187, 7, v166
	v_min_u32_e32 v187, 11, v187
	v_lshlrev_b32_e32 v187, 2, v187
	s_cmp_eq_u32 s15, 7
	s_cselect_b32 s22, 0, 0x20000
	s_add_u32 s84, s18, s22
	s_addc_u32 s85, s19, 0
	s_add_u32 s86, s18, s22
	s_addc_u32 s87, s19, 0
	s_add_u32 s86, s86, 0x1000
	s_addc_u32 s87, s87, 0
	s_add_u32 s88, s20, s22
	s_addc_u32 s89, s21, 0
	s_add_u32 s90, s20, s22
	s_addc_u32 s91, s21, 0
	s_add_u32 s90, s90, 0x1000
	s_addc_u32 s91, s91, 0
	s_waitcnt lgkmcnt(0)
	v_writelane_b32 v171, s40, 0
	v_writelane_b32 v171, s41, 1
	v_writelane_b32 v171, s42, 2
	v_writelane_b32 v171, s43, 3
	v_writelane_b32 v171, s44, 4
	v_writelane_b32 v171, s45, 5
	v_writelane_b32 v171, s46, 6
	v_writelane_b32 v171, s47, 7
	v_writelane_b32 v171, s48, 8
	v_writelane_b32 v171, s49, 9
	v_writelane_b32 v171, s50, 10
	v_writelane_b32 v171, 0, 11
	v_fma_mixlo_f16 v171, v171, s51, 0
	ds_bpermute_b32 v188, v172, v171
	ds_bpermute_b32 v189, v173, v171
	ds_bpermute_b32 v190, v174, v171
	ds_bpermute_b32 v191, v175, v171
	ds_bpermute_b32 v192, v176, v171
	ds_bpermute_b32 v193, v177, v171
	ds_bpermute_b32 v194, v178, v171
	ds_bpermute_b32 v195, v179, v171
	v_mov_b32_e32 v229, 0x44800000
	v_fma_mixlo_f16 v228, s40, v229, 0
	v_cvt_f32_f16_e32 v228, v228
	v_cvt_f64_f32_e32 v[212:213], v228
	v_add_f64 v[212:213], v[212:213], 0
	v_fma_mixlo_f16 v228, s41, v229, 0
	v_cvt_f32_f16_e32 v228, v228
	v_cvt_f64_f32_e32 v[214:215], v228
	v_add_f64 v[212:213], v[212:213], v[214:215]
	v_fma_mixlo_f16 v228, s42, v229, 0
	v_cvt_f32_f16_e32 v228, v228
	v_cvt_f64_f32_e32 v[214:215], v228
	v_add_f64 v[212:213], v[212:213], v[214:215]
	v_fma_mixlo_f16 v228, s43, v229, 0
	v_cvt_f32_f16_e32 v228, v228
	v_cvt_f64_f32_e32 v[214:215], v228
	v_add_f64 v[212:213], v[212:213], v[214:215]
	v_fma_mixlo_f16 v228, s44, v229, 0
	v_cvt_f32_f16_e32 v228, v228
	v_cvt_f64_f32_e32 v[214:215], v228
	v_add_f64 v[212:213], v[212:213], v[214:215]
	v_fma_mixlo_f16 v228, s45, v229, 0
	v_cvt_f32_f16_e32 v228, v228
	v_cvt_f64_f32_e32 v[214:215], v228
	v_add_f64 v[212:213], v[212:213], v[214:215]
	v_fma_mixlo_f16 v228, s46, v229, 0
	v_cvt_f32_f16_e32 v228, v228
	v_cvt_f64_f32_e32 v[214:215], v228
	v_add_f64 v[212:213], v[212:213], v[214:215]
	v_fma_mixlo_f16 v228, s47, v229, 0
	v_cvt_f32_f16_e32 v228, v228
	v_cvt_f64_f32_e32 v[214:215], v228
	v_add_f64 v[212:213], v[212:213], v[214:215]
	v_fma_mixlo_f16 v228, s48, v229, 0
	v_cvt_f32_f16_e32 v228, v228
	v_cvt_f64_f32_e32 v[214:215], v228
	v_add_f64 v[212:213], v[212:213], v[214:215]
	v_fma_mixlo_f16 v228, s49, v229, 0
	v_cvt_f32_f16_e32 v228, v228
	v_cvt_f64_f32_e32 v[214:215], v228
	v_add_f64 v[212:213], v[212:213], v[214:215]
	v_fma_mixlo_f16 v228, s50, v229, 0
	v_cvt_f32_f16_e32 v228, v228
	v_cvt_f64_f32_e32 v[214:215], v228
	v_add_f64 v[212:213], v[212:213], v[214:215]
	s_waitcnt lgkmcnt(7)
	ds_bpermute_b32 v196, v180, v171
	ds_bpermute_b32 v197, v181, v171
	ds_bpermute_b32 v198, v182, v171
	ds_bpermute_b32 v199, v183, v171
	ds_bpermute_b32 v200, v184, v171
	ds_bpermute_b32 v201, v185, v171
	ds_bpermute_b32 v202, v186, v171
	ds_bpermute_b32 v203, v187, v171
	v_mul_f64 v[212:213], v[212:213], v[212:213]
	v_mul_f64 v[216:217], v[212:213], 0.5
	v_add_f64 v[218:219], v[216:217], v[216:217]
	s_mov_b32 s36, 0xeb1c432d
	s_mov_b32 s37, 0x3f1a36e2
	v_mul_f64 v[220:221], v[212:213], s[36:37]
	v_mul_f64 v[222:223], v[216:217], v[218:219]
	v_fmac_f64_e32 v[222:223], v[212:213], v[220:221]
	v_add_f64 v[224:225], v[212:213], v[212:213]
	s_mov_b32 s36, 0x487fcb92
	s_mov_b32 s37, 0x3f4d7dbf
	v_mul_f64 v[226:227], v[212:213], s[36:37]
	v_cvt_f32_f64_e32 v0, v[226:227]
	v_mov_b32_e32 v1, v0
	v_mov_b32_e32 v2, v0
	v_mov_b32_e32 v3, v0
	v_cvt_f32_f64_e32 v10, v[218:219]
	v_cvt_f32_f64_e32 v11, v[222:223]
	v_cvt_f32_f64_e32 v12, v[212:213]
	v_cvt_f32_f64_e32 v13, v[224:225]
	v_mul_f64 v[226:227], v[212:213], v[226:227]
	v_cvt_f32_f64_e32 v14, v[226:227]
	v_lshlrev_b32_e32 v167, 2, v164
	s_cmp_eq_u32 s12, 0
	s_cselect_b32 s23, 6, 64
	v_add_u32_e32 v168, 0, v167
	v_cmp_gt_u32_e32 vcc, s23, v168
	s_nop 1
	v_cndmask_b32_e64 v15, 0, 1.0, vcc
	v_add_u32_e32 v168, 1, v167
	v_cmp_gt_u32_e32 vcc, s23, v168
	s_nop 1
	v_cndmask_b32_e64 v16, 0, 1.0, vcc
	v_add_u32_e32 v168, 2, v167
	v_cmp_gt_u32_e32 vcc, s23, v168
	s_nop 1
	v_cndmask_b32_e64 v17, 0, 1.0, vcc
	v_add_u32_e32 v168, 3, v167
	v_cmp_gt_u32_e32 vcc, s23, v168
	s_nop 1
	v_cndmask_b32_e64 v18, 0, 1.0, vcc
	v_and_b32_e32 v167, 31, v8
	v_lshlrev_b32_e32 v167, 4, v167
	s_lshl_b32 s24, s12, 11
	s_add_i32 s25, s12, 7
	s_and_b32 s25, s25, 7
	s_lshl_b32 s26, s25, 11
	v_or_b32_e32 v4, s24, v167
	v_or_b32_e32 v5, s26, v167
	s_lshl_b32 s28, s25, 2
	s_add_u32 s28, s28, 0x10000
	v_mov_b32_e32 v7, s28
	v_mov_b32_e32 v19, 0
	v_mov_b32_e32 v20, 0
	v_mov_b32_e32 v21, 0
	v_mov_b32_e32 v22, 0
	s_waitcnt lgkmcnt(0)
	v_cmp_lt_u32_e64 s[32:33], 31, v8
	v_cmp_gt_u32_e64 s[34:35], 32, v8
	v_pack_b32_f16 v24, v188, v189
	v_pack_b32_f16 v25, v190, v191
	v_pack_b32_f16 v26, v192, v193
	v_pack_b32_f16 v27, v194, v195
	v_pack_b32_f16 v167, v196, v197
	v_cndmask_b32_e64 v28, 0, v167, s[32:33]
	v_cndmask_b32_e64 v32, 0, v167, s[34:35]
	v_pack_b32_f16 v167, v198, v199
	v_cndmask_b32_e64 v29, 0, v167, s[32:33]
	v_cndmask_b32_e64 v33, 0, v167, s[34:35]
	v_pack_b32_f16 v167, v200, v201
	v_cndmask_b32_e64 v30, 0, v167, s[32:33]
	v_cndmask_b32_e64 v34, 0, v167, s[34:35]
	v_pack_b32_f16 v167, v202, v203
	v_cndmask_b32_e64 v31, 0, v167, s[32:33]
	v_cndmask_b32_e64 v35, 0, v167, s[34:35]
	s_waitcnt lgkmcnt(0)
	s_barrier
	s_cmp_lt_u32 s12, 4
	s_cbranch_scc0 .Lq_noprio
	s_setprio 1
